# v42 + instruction selection in the MLA softmax: 30 scalar v_fmamk_f32 become 15 v_pk_fma_f32 (same fused rounding, bit-identical)
# baseline (speedup 1.0000x reference)
.LBB0_651:
	s_and_b32 s2, s18, 7
	s_bfe_u32 s20, s19, 0x20003
	s_mul_i32 s4, s2, 0x60000
	s_mul_i32 s0, s20, 0x180
	s_or_b32 s4, s4, s0
	s_add_u32 s8, s14, s4
	s_addc_u32 s9, s15, 0
	s_lshl_b32 s2, s2, 19
	s_lshl_b32 s12, s20, 9
	s_or_b32 s2, s2, s12
	s_add_u32 s10, s16, s2
	s_getreg_b32 s2, hwreg(HW_REG_HW_ID, 0, 6)
	s_addc_u32 s11, s17, 0
	s_and_b32 s2, s2, 63
	s_lshl_b32 s2, s2, 2
	s_add_i32 s2, s2, 0
	s_add_i32 s2, s2, 0x20010
	v_mov_b32_e32 v0, s2
	ds_read_b32 v0, v0
	s_and_b32 s13, s19, 7
	s_lshl_b32 s4, s19, 3
	s_lshl_b32 s2, s13, 11
	s_and_b32 s4, s4, 0xffffff00
	s_add_i32 s2, s2, s4
	s_waitcnt lgkmcnt(0)
	v_readfirstlane_b32 s4, v0
	s_mov_b32 s98, 0x3dd53b94
	s_lshl_b32 s24, s4, 6
	s_waitcnt vmcnt(1)
	v_mbcnt_lo_u32_b32 v23, -1, 0
	v_mbcnt_hi_u32_b32 v23, -1, v23
	v_readlane_b32 s4, v255, 5
	s_waitcnt vmcnt(0)
	v_or_b32_e32 v18, s24, v23
	v_ashrrev_i32_e32 v0, 1, v18
	v_and_b32_e32 v0, 0xffffffe0, v0
	v_and_b32_e32 v189, 31, v23
	v_add_u32_e32 v168, s2, v0
	v_readlane_b32 s5, v255, 6
	v_or_b32_e32 v2, v168, v189
	s_movk_i32 s25, 0x600
	v_mov_b64_e32 v[0:1], s[4:5]
	s_lshl_b32 s2, s13, 8
	v_mad_i64_i32 v[0:1], s[4:5], v2, s25, v[0:1]
	s_bitset1_b32 s2, 14
	s_mul_i32 s4, s2, 0x600
	v_readlane_b32 s21, v255, 7
	s_add_u32 s4, s21, s4
	v_readlane_b32 s22, v255, 8
	s_addc_u32 s5, s22, 0
	s_add_u32 s4, s4, s0
	s_addc_u32 s5, s5, 0
	s_lshl_b32 s2, s2, 11
	v_readlane_b32 s23, v255, 9
	s_add_u32 s2, s23, s2
	v_readlane_b32 s26, v255, 10
	s_addc_u32 s7, s26, 0
	v_lshlrev_b32_e32 v28, 3, v23
	v_add_u32_e32 v12, 0x200, v18
	v_bfe_u32 v188, v23, 5, 1
	s_add_u32 s6, s2, s12
	v_and_b32_e32 v22, 0x78, v28
	v_ashrrev_i32_e32 v24, 4, v18
	v_ashrrev_i32_e32 v26, 4, v12
	v_lshl_add_u64 v[0:1], v[0:1], 0, s[0:1]
	v_lshlrev_b32_e32 v170, 4, v188
	v_mov_b32_e32 v171, v97
	s_addc_u32 s7, s7, 0
	v_lshlrev_b32_e32 v96, 1, v22
	v_ashrrev_i32_e32 v25, 31, v24
	v_ashrrev_i32_e32 v27, 31, v26
	v_lshl_add_u64 v[20:21], v[0:1], 0, v[170:171]
	v_lshl_add_u64 v[0:1], s[6:7], 0, v[96:97]
	v_lshlrev_b64 v[172:173], 11, v[24:25]
	v_lshlrev_b64 v[174:175], 11, v[26:27]
	v_lshl_add_u64 v[2:3], v[0:1], 0, v[172:173]
	v_lshl_add_u64 v[4:5], v[0:1], 0, v[174:175]
	s_mov_b32 s2, 0x2aaaaaab
	global_load_dwordx4 v[102:105], v[20:21], off
	global_load_dwordx4 v[98:101], v[20:21], off offset:32
	s_nop 0
	global_load_dwordx4 v[0:3], v[2:3], off offset:256
	s_nop 0
	global_load_dwordx4 v[4:7], v[4:5], off offset:256
	v_mul_hi_i32 v8, v18, s2
	v_lshrrev_b32_e32 v9, 31, v8
	v_ashrrev_i32_e32 v8, 2, v8
	v_add_u32_e32 v25, v8, v9
	v_mul_lo_u32 v10, v25, 24
	v_sub_u32_e32 v27, v18, v10
	v_mul_hi_i32 v10, v12, s2
	v_lshrrev_b32_e32 v11, 31, v10
	v_ashrrev_i32_e32 v10, 2, v10
	v_add_u32_e32 v29, v10, v11
	v_mul_lo_u32 v13, v29, 24
	v_sub_u32_e32 v30, v12, v13
	v_mov_b64_e32 v[16:17], s[4:5]
	v_lshlrev_b32_e32 v176, 3, v27
	v_lshlrev_b32_e32 v178, 3, v30
	v_mad_i64_i32 v[8:9], s[4:5], v25, s25, v[16:17]
	v_ashrrev_i32_e32 v177, 31, v176
	v_mad_i64_i32 v[10:11], s[4:5], v29, s25, v[16:17]
	v_ashrrev_i32_e32 v179, 31, v178
	v_lshl_add_u64 v[8:9], v[176:177], 1, v[8:9]
	v_lshl_add_u64 v[12:13], v[178:179], 1, v[10:11]
	global_load_dwordx4 v[8:11], v[8:9], off
	s_nop 0
	global_load_dwordx4 v[12:15], v[12:13], off
	v_add_u32_e32 v18, 0x400, v18
	v_mul_hi_i32 v19, v18, s2
	v_lshrrev_b32_e32 v31, 31, v19
	v_ashrrev_i32_e32 v19, 2, v19
	v_add_u32_e32 v31, v19, v31
	v_mul_lo_u32 v19, v31, 24
	v_sub_u32_e32 v32, v18, v19
	v_lshlrev_b32_e32 v180, 3, v32
	v_mad_i64_i32 v[16:17], s[4:5], v31, s25, v[16:17]
	v_ashrrev_i32_e32 v181, 31, v180
	v_lshl_add_u64 v[16:17], v[180:181], 1, v[16:17]
	global_load_dwordx4 v[16:19], v[16:17], off
	s_nop 0
	global_load_dwordx4 v[142:145], v[20:21], off offset:64
	global_load_dwordx4 v[138:141], v[20:21], off offset:96
	global_load_dwordx4 v[134:137], v[20:21], off offset:128
	global_load_dwordx4 v[130:133], v[20:21], off offset:160
	global_load_dwordx4 v[126:129], v[20:21], off offset:192
	global_load_dwordx4 v[122:125], v[20:21], off offset:224
	global_load_dwordx4 v[118:121], v[20:21], off offset:256
	global_load_dwordx4 v[114:117], v[20:21], off offset:288
	global_load_dwordx4 v[110:113], v[20:21], off offset:320
	global_load_dwordx4 v[106:109], v[20:21], off offset:352
	v_lshlrev_b32_e32 v21, 4, v23
	v_and_b32_e32 v34, 0xc0, v21
	v_and_b32_e32 v198, 48, v21
	v_and_b32_e32 v21, 0xfffff0, v24
	v_lshlrev_b32_e32 v36, 1, v24
	v_and_or_b32 v21, v36, 8, v21
	v_bfe_u32 v35, v28, 5, 2
	v_lshrrev_b32_e32 v21, 1, v21
	v_or_b32_e32 v21, v21, v35
	v_lshrrev_b32_e32 v36, 1, v24
	v_lshlrev_b32_e32 v200, 9, v21
	v_and_b32_e32 v21, 3, v24
	v_and_or_b32 v21, v36, 4, v21
	v_lshlrev_b32_e32 v202, 6, v21
	v_add_u32_e32 v21, 0, v200
	v_add3_u32 v21, v21, v202, v198
	s_mul_i32 s2, s13, 0x300000
	s_waitcnt vmcnt(0)
	s_add_u32 s2, s21, s2
	s_addc_u32 s4, s22, 0
	s_add_u32 s2, s2, s0
	s_addc_u32 s21, s4, 0
	s_lshl_b32 s0, s13, 22
	s_add_u32 s0, s23, s0
	s_addc_u32 s4, s26, 0
	s_add_u32 s22, s0, s12
	v_mov_b32_e32 v20, 0x3fffffc0
	s_addc_u32 s23, s4, 0
	v_bitop3_b32 v20, s24, v20, v23 bitop3:0xc8
	s_add_i32 s0, 0, 0x14000
	v_lshl_add_u32 v171, v20, 2, s0
	s_movk_i32 s0, 0x180
	v_mul_lo_u32 v207, v25, s0
	v_mul_lo_u32 v229, v29, s0
	v_mul_lo_u32 v231, v31, s0
	v_lshlrev_b32_e32 v33, 1, v23
	s_cmp_lg_u32 0, -1
	v_and_b32_e32 v20, 63, v23
	v_mad_i64_i32 v[182:183], s[4:5], v25, s25, 0
	v_mad_i64_i32 v[184:185], s[4:5], v29, s25, 0
	s_waitcnt vmcnt(14)
	ds_write_b128 v21, v[0:3]
	v_and_b32_e32 v0, 0xfffff0, v26
	v_lshlrev_b32_e32 v1, 1, v26
	v_and_or_b32 v0, v1, 8, v0
	v_lshrrev_b32_e32 v0, 1, v0
	v_or_b32_e32 v0, v0, v35
	v_lshrrev_b32_e32 v1, 1, v26
	v_lshlrev_b32_e32 v204, 9, v0
	v_and_b32_e32 v0, 3, v26
	v_and_or_b32 v0, v1, 4, v0
	v_lshlrev_b32_e32 v205, 6, v0
	v_add_u32_e32 v0, 0, v204
	v_add3_u32 v0, v0, v205, v198
	s_waitcnt vmcnt(13)
	ds_write_b128 v0, v[4:7]
	v_lshrrev_b32_e32 v0, 1, v25
	v_bitop3_b32 v0, v0, v27, 7 bitop3:0x6c
	v_lshlrev_b32_e32 v227, 4, v0
	v_add3_u32 v0, 0, v227, v207
	v_bfe_u32 v1, v23, 1, 3
	v_mad_i64_i32 v[186:187], s[4:5], v31, s25, 0
	s_cselect_b32 s0, 0, 0
	v_cmp_gt_u32_e64 s[4:5], 32, v20
	s_waitcnt vmcnt(12)
	ds_write_b128 v0, v[8:11] offset:32768
	v_lshrrev_b32_e32 v0, 1, v29
	v_bitop3_b32 v0, v0, v30, 7 bitop3:0x6c
	v_lshlrev_b32_e32 v230, 4, v0
	v_add3_u32 v0, 0, v230, v229
	s_waitcnt vmcnt(11)
	ds_write_b128 v0, v[12:15] offset:32768
	v_lshrrev_b32_e32 v0, 1, v31
	v_bitop3_b32 v0, v0, v32, 7 bitop3:0x6c
	v_lshlrev_b32_e32 v233, 4, v0
	v_add3_u32 v0, 0, v233, v231
	s_waitcnt vmcnt(10)
	ds_write_b128 v0, v[16:19] offset:32768
	v_lshrrev_b32_e32 v0, 1, v23
	v_bitop3_b32 v0, v188, v0, 7 bitop3:0x78
	v_lshlrev_b32_e32 v235, 4, v0
	v_bitop3_b32 v0, v188, v1, 2 bitop3:0x36
	v_lshlrev_b32_e32 v232, 4, v0
	v_bitop3_b32 v0, v188, v1, 4 bitop3:0x36
	v_lshlrev_b32_e32 v228, 4, v0
	v_bitop3_b32 v0, v188, v1, 6 bitop3:0x36
	v_lshlrev_b32_e32 v206, 4, v0
	v_bitop3_b32 v0, v188, v1, 8 bitop3:0x36
	v_lshlrev_b32_e32 v203, 4, v0
	v_bitop3_b32 v0, v188, v1, 10 bitop3:0x36
	v_lshlrev_b32_e32 v201, 4, v0
	v_bitop3_b32 v0, v188, v1, 12 bitop3:0x36
	v_lshlrev_b32_e32 v199, 4, v0
	v_bitop3_b32 v0, v188, v1, 14 bitop3:0x36
	v_lshlrev_b32_e32 v196, 4, v0
	v_bitop3_b32 v0, v188, v1, 16 bitop3:0x36
	v_lshlrev_b32_e32 v195, 4, v0
	v_bitop3_b32 v0, v188, v1, 18 bitop3:0x36
	v_lshlrev_b32_e32 v194, 4, v0
	v_bitop3_b32 v0, v188, v1, 20 bitop3:0x36
	v_lshlrev_b32_e32 v193, 4, v0
	v_bitop3_b32 v0, v188, v1, 22 bitop3:0x36
	v_lshlrev_b32_e32 v192, 4, v0
	v_and_b32_e32 v0, 0x118, v28
	v_and_or_b32 v0, v33, 32, v0
	v_mov_b32_e32 v14, v97
	v_mov_b32_e32 v15, v97
	v_add3_u32 v190, v34, s0, v0
	v_mov_b32_e32 v0, v97
	v_mov_b32_e32 v1, v97
	v_mov_b32_e32 v2, v97
	v_mov_b32_e32 v3, v97
	v_mov_b32_e32 v4, v97
	v_mov_b32_e32 v5, v97
	v_mov_b32_e32 v6, v97
	v_mov_b32_e32 v7, v97
	v_mov_b32_e32 v8, v97
	v_mov_b32_e32 v9, v97
	v_mov_b32_e32 v10, v97
	v_mov_b32_e32 v11, v97
	v_mov_b32_e32 v12, v97
	v_mov_b32_e32 v13, v97
	v_lshlrev_b32_e32 v96, 1, v22
	v_mov_b64_e32 v[30:31], v[14:15]
	v_mov_b64_e32 v[46:47], v[14:15]
	v_mov_b64_e32 v[62:63], v[14:15]
	v_mul_u32_u24_e32 v234, 0x180, v189
	v_lshl_add_u32 v169, v189, 2, v171
	v_mov_b32_e32 v191, 0xf149f2ca
	v_mov_b32_e32 v236, 0
	s_mov_b32 s0, -3
	v_mov_b64_e32 v[28:29], v[12:13]
	v_mov_b64_e32 v[26:27], v[10:11]
	v_mov_b64_e32 v[24:25], v[8:9]
	v_mov_b64_e32 v[22:23], v[6:7]
	v_mov_b64_e32 v[20:21], v[4:5]
	v_mov_b64_e32 v[18:19], v[2:3]
	v_mov_b64_e32 v[16:17], v[0:1]
	v_mov_b64_e32 v[44:45], v[12:13]
	v_mov_b64_e32 v[42:43], v[10:11]
	v_mov_b64_e32 v[40:41], v[8:9]
	v_mov_b64_e32 v[38:39], v[6:7]
	v_mov_b64_e32 v[36:37], v[4:5]
	v_mov_b64_e32 v[34:35], v[2:3]
	v_mov_b64_e32 v[32:33], v[0:1]
	v_mov_b64_e32 v[60:61], v[12:13]
	v_mov_b64_e32 v[58:59], v[10:11]
	v_mov_b64_e32 v[56:57], v[8:9]
	v_mov_b64_e32 v[54:55], v[6:7]
	v_mov_b64_e32 v[52:53], v[4:5]
	v_mov_b64_e32 v[50:51], v[2:3]
	v_mov_b64_e32 v[48:49], v[0:1]
	s_waitcnt lgkmcnt(0)
	s_barrier

.LBB0_660:
	v_cndmask_b32_e64 v191, v197, v191, s[6:7]
	v_mul_f32_e32 v166, 0xbdd53b94, v191
	v_pk_fma_f32 v[80:81], v[80:81], s[98:99], v[166:167] op_sel_hi:[1,0,0]
	v_pk_fma_f32 v[82:83], v[82:83], s[98:99], v[166:167] op_sel_hi:[1,0,0]
	v_pk_fma_f32 v[84:85], v[84:85], s[98:99], v[166:167] op_sel_hi:[1,0,0]
	v_pk_fma_f32 v[86:87], v[86:87], s[98:99], v[166:167] op_sel_hi:[1,0,0]
	v_pk_fma_f32 v[88:89], v[88:89], s[98:99], v[166:167] op_sel_hi:[1,0,0]
	v_pk_fma_f32 v[90:91], v[90:91], s[98:99], v[166:167] op_sel_hi:[1,0,0]
	v_pk_fma_f32 v[92:93], v[92:93], s[98:99], v[166:167] op_sel_hi:[1,0,0]
	v_pk_fma_f32 v[94:95], v[94:95], s[98:99], v[166:167] op_sel_hi:[1,0,0]
	v_pk_fma_f32 v[64:65], v[64:65], s[98:99], v[166:167] op_sel_hi:[1,0,0]
	v_pk_fma_f32 v[66:67], v[66:67], s[98:99], v[166:167] op_sel_hi:[1,0,0]
	v_pk_fma_f32 v[68:69], v[68:69], s[98:99], v[166:167] op_sel_hi:[1,0,0]
	v_pk_fma_f32 v[70:71], v[70:71], s[98:99], v[166:167] op_sel_hi:[1,0,0]
	v_pk_fma_f32 v[72:73], v[72:73], s[98:99], v[166:167] op_sel_hi:[1,0,0]
	v_pk_fma_f32 v[74:75], v[74:75], s[98:99], v[166:167] op_sel_hi:[1,0,0]
	v_pk_fma_f32 v[76:77], v[76:77], s[98:99], v[166:167] op_sel_hi:[1,0,0]
	v_fmamk_f32 v78, v78, 0x3dd53b94, v166
	v_fmac_f32_e32 v166, 0x3dd53b94, v79
	v_exp_f32_e32 v79, v80
	v_exp_f32_e32 v80, v81
	v_exp_f32_e32 v81, v82
	v_exp_f32_e32 v82, v83
	v_exp_f32_e32 v83, v84
	v_exp_f32_e32 v84, v85
	v_exp_f32_e32 v85, v86
	v_exp_f32_e32 v86, v87
	v_exp_f32_e32 v87, v88
	v_exp_f32_e32 v88, v89
	v_exp_f32_e32 v89, v90
	v_exp_f32_e32 v90, v91
	v_exp_f32_e32 v91, v92
	v_exp_f32_e32 v92, v93
	v_exp_f32_e32 v93, v94
	v_exp_f32_e32 v94, v95
	v_exp_f32_e32 v95, v64
	v_add_f32_e32 v64, 0, v79
	v_add_f32_e32 v64, v80, v64
	v_add_f32_e32 v64, v81, v64
	v_add_f32_e32 v64, v82, v64
	v_add_f32_e32 v64, v83, v64
	v_add_f32_e32 v64, v84, v64
	v_add_f32_e32 v64, v85, v64
	v_add_f32_e32 v64, v86, v64
	v_add_f32_e32 v64, v87, v64
	v_add_f32_e32 v64, v88, v64
	v_add_f32_e32 v64, v89, v64
	v_add_f32_e32 v64, v90, v64
	v_add_f32_e32 v64, v91, v64
	v_exp_f32_e32 v167, v65
	v_add_f32_e32 v64, v92, v64
	v_exp_f32_e32 v208, v66
	v_add_f32_e32 v64, v93, v64
	v_exp_f32_e32 v209, v67
	v_add_f32_e32 v64, v94, v64
	v_exp_f32_e32 v210, v68
	v_add_f32_e32 v64, v95, v64
	v_exp_f32_e32 v211, v69
	v_add_f32_e32 v64, v167, v64
	v_exp_f32_e32 v214, v70
	v_add_f32_e32 v64, v208, v64
	v_exp_f32_e32 v215, v71
	v_add_f32_e32 v64, v209, v64
	v_exp_f32_e32 v216, v72
	v_add_f32_e32 v64, v210, v64
	v_exp_f32_e32 v217, v73
	v_add_f32_e32 v64, v211, v64
	v_exp_f32_e32 v218, v74
	v_add_f32_e32 v64, v214, v64
	v_exp_f32_e32 v220, v75
	v_add_f32_e32 v64, v215, v64
	v_exp_f32_e32 v221, v76
	v_add_f32_e32 v64, v216, v64
	v_exp_f32_e32 v222, v77
	v_add_f32_e32 v64, v217, v64
	v_exp_f32_e32 v223, v78
	v_add_f32_e32 v64, v218, v64
	v_exp_f32_e32 v166, v166
	v_add_f32_e32 v64, v220, v64
	v_add_f32_e32 v64, v221, v64
	v_add_f32_e32 v64, v222, v64
	v_add_f32_e32 v64, v223, v64
	v_add_f32_e32 v64, v166, v64
	v_mov_b32_e32 v65, v64
	s_nop 1
	v_permlane32_swap_b32_e32 v64, v65
	v_add_f32_e32 v197, v64, v65
	v_fmac_f32_e32 v197, v236, v237
	v_cvt_pk_bf16_f32 v64, v79, v80
	v_cvt_pk_bf16_f32 v65, v81, v82
	v_cvt_pk_bf16_f32 v66, v83, v84
	v_cvt_pk_bf16_f32 v67, v85, v86
	v_cvt_pk_bf16_f32 v68, v87, v88
	v_cvt_pk_bf16_f32 v69, v89, v90
	v_cvt_pk_bf16_f32 v70, v91, v92
	v_cvt_pk_bf16_f32 v71, v93, v94
	v_cvt_pk_bf16_f32 v72, v95, v167
	v_cvt_pk_bf16_f32 v73, v208, v209
	v_cvt_pk_bf16_f32 v74, v210, v211
	v_cvt_pk_bf16_f32 v75, v214, v215
	v_cvt_pk_bf16_f32 v76, v216, v217
	v_cvt_pk_bf16_f32 v77, v218, v220
	v_cvt_pk_bf16_f32 v78, v221, v222
	v_cvt_pk_bf16_f32 v79, v223, v166
	s_nop 0
	v_permlane32_swap_b32_e32 v64, v66
	v_permlane32_swap_b32_e32 v65, v67
	v_permlane32_swap_b32_e32 v68, v70
	v_permlane32_swap_b32_e32 v69, v71
	v_permlane32_swap_b32_e32 v72, v74
	v_permlane32_swap_b32_e32 v73, v75
	v_permlane32_swap_b32_e32 v76, v78
	v_permlane32_swap_b32_e32 v77, v79
	s_lshl_b32 s6, s24, 14
	v_add_u32_e32 v166, s6, v190
	ds_read_b64_tr_b16 v[80:81], v166 offset:0
	ds_read_b64_tr_b16 v[82:83], v166 offset:0x800
	ds_read_b64_tr_b16 v[84:85], v166 offset:0x1000
	ds_read_b64_tr_b16 v[86:87], v166 offset:0x1800
	ds_read_b64_tr_b16 v[88:89], v166 offset:0x2000
	ds_read_b64_tr_b16 v[90:91], v166 offset:0x2800
	ds_read_b64_tr_b16 v[92:93], v166 offset:0x3000
	ds_read_b64_tr_b16 v[94:95], v166 offset:0x3800
	s_waitcnt lgkmcnt(0)
	s_nop 0
	v_mfma_f32_32x32x16_bf16 v[48:63], v[64:67], v[80:83], v[48:63]
	ds_read_b64_tr_b16 v[80:81], v166 offset:0x200
	ds_read_b64_tr_b16 v[82:83], v166 offset:0xa00
	v_mfma_f32_32x32x16_bf16 v[48:63], v[68:71], v[84:87], v[48:63]
	ds_read_b64_tr_b16 v[84:85], v166 offset:0x1200
	ds_read_b64_tr_b16 v[86:87], v166 offset:0x1a00
	v_mfma_f32_32x32x16_bf16 v[48:63], v[72:75], v[88:91], v[48:63]
	ds_read_b64_tr_b16 v[88:89], v166 offset:0x2200
	ds_read_b64_tr_b16 v[90:91], v166 offset:0x2a00
	v_mfma_f32_32x32x16_bf16 v[48:63], v[76:79], v[92:95], v[48:63]
	ds_read_b64_tr_b16 v[92:93], v166 offset:0x3200
	ds_read_b64_tr_b16 v[94:95], v166 offset:0x3a00
	s_waitcnt lgkmcnt(0)
	v_mfma_f32_32x32x16_bf16 v[32:47], v[64:67], v[80:83], v[32:47]
	ds_read_b64_tr_b16 v[80:81], v166 offset:0x400
	ds_read_b64_tr_b16 v[82:83], v166 offset:0xc00
	v_mfma_f32_32x32x16_bf16 v[32:47], v[68:71], v[84:87], v[32:47]
	ds_read_b64_tr_b16 v[84:85], v166 offset:0x1400
	ds_read_b64_tr_b16 v[86:87], v166 offset:0x1c00
	v_mfma_f32_32x32x16_bf16 v[32:47], v[72:75], v[88:91], v[32:47]
	ds_read_b64_tr_b16 v[88:89], v166 offset:0x2400
	ds_read_b64_tr_b16 v[90:91], v166 offset:0x2c00
	v_mfma_f32_32x32x16_bf16 v[32:47], v[76:79], v[92:95], v[32:47]
	ds_read_b64_tr_b16 v[92:93], v166 offset:0x3400
	ds_read_b64_tr_b16 v[94:95], v166 offset:0x3c00
	s_waitcnt lgkmcnt(0)
	v_mfma_f32_32x32x16_bf16 v[16:31], v[64:67], v[80:83], v[16:31]
	ds_read_b64_tr_b16 v[80:81], v166 offset:0x600
	ds_read_b64_tr_b16 v[82:83], v166 offset:0xe00
	v_mfma_f32_32x32x16_bf16 v[16:31], v[68:71], v[84:87], v[16:31]
	ds_read_b64_tr_b16 v[84:85], v166 offset:0x1600
	ds_read_b64_tr_b16 v[86:87], v166 offset:0x1e00
	v_mfma_f32_32x32x16_bf16 v[16:31], v[72:75], v[88:91], v[16:31]
	ds_read_b64_tr_b16 v[88:89], v166 offset:0x2600
	ds_read_b64_tr_b16 v[90:91], v166 offset:0x2e00
	v_mfma_f32_32x32x16_bf16 v[16:31], v[76:79], v[92:95], v[16:31]
	ds_read_b64_tr_b16 v[92:93], v166 offset:0x3600
	ds_read_b64_tr_b16 v[94:95], v166 offset:0x3e00
	s_waitcnt lgkmcnt(0)
	v_mfma_f32_32x32x16_bf16 v[0:15], v[64:67], v[80:83], v[0:15]
	s_xor_b32 s6, s6, 0x4000
	s_add_i32 s6, s6, 0
	v_add_u32_e32 v64, s6, v200
	v_add3_u32 v64, v64, v202, v198
	s_waitcnt vmcnt(0)
	s_waitcnt vmcnt(4)
	ds_write_b128 v64, v[162:165]
	v_add_u32_e32 v64, s6, v204
	v_mfma_f32_32x32x16_bf16 v[0:15], v[68:71], v[84:87], v[0:15]
	s_xor_b32 s6, s24, 1
	s_mulk_i32 s6, 0x6000
	s_add_i32 s6, s6, 0
	s_add_i32 s0, s0, 1
	s_add_u32 s8, s8, 0x18000
	v_add3_u32 v64, v64, v205, v198
	s_addc_u32 s9, s9, 0
	v_mfma_f32_32x32x16_bf16 v[0:15], v[72:75], v[88:91], v[0:15]
	s_waitcnt vmcnt(3)
	ds_write_b128 v64, v[158:161]
	v_add3_u32 v64, s6, v227, v207
	s_add_u32 s10, s10, 0x20000
	s_waitcnt vmcnt(2)
	ds_write_b128 v64, v[150:153] offset:32768
	v_add3_u32 v64, s6, v230, v229
	s_addc_u32 s11, s11, 0
	s_waitcnt vmcnt(1)
	ds_write_b128 v64, v[146:149] offset:32768
	v_mfma_f32_32x32x16_bf16 v[0:15], v[76:79], v[92:95], v[0:15]
	v_add3_u32 v64, s6, v233, v231
	s_cmp_lg_u32 s0, 32
	s_waitcnt vmcnt(0)
	ds_write_b128 v64, v[154:157] offset:32768
	s_waitcnt lgkmcnt(0)
	s_barrier
	s_cbranch_scc0 .LBB0_662
	v_mov_b32_e32 v236, v197
	s_branch .LBB0_652
